# P3 knorm: per-row xor-8/4/2/1 butterflies as DPP moves instead of ds_bpermute (bit-identical)
# baseline (speedup 1.0000x reference)
.LBB0_347:
	s_ashr_i32 s0, s4, 10
	s_ashr_i32 s1, s0, 31
	s_and_b32 s49, s5, 0x1fc0
	s_lshl_b64 s[0:1], s[0:1], 13
	v_or_b32_e32 v2, s49, v1
	v_or_b32_e32 v2, s0, v2
	s_and_b32 s6, s4, 0x380
	s_waitcnt lgkmcnt(0)
	v_mad_u64_u32 v[2:3], s[54:55], v2, s14, v[8:9]
	v_mad_i32_i24 v3, s1, v18, v3
	s_lshl_b32 s6, s6, 1
	v_lshl_add_u64 v[2:3], v[2:3], 0, s[6:7]
	v_lshl_add_u64 v[10:11], v[2:3], 0, v[6:7]
	v_add_co_u32_e64 v2, s[0:1], s15, v10
	s_nop 1
	v_addc_co_u32_e64 v3, s[0:1], 0, v11, s[0:1]
	global_load_dwordx4 v[20:23], v[2:3], off offset:2048
	v_add_co_u32_e64 v2, s[0:1], s16, v10
	s_waitcnt vmcnt(0)
	v_lshlrev_b32_e32 v19, 16, v20
	v_addc_co_u32_e64 v3, s[0:1], 0, v11, s[0:1]
	global_load_dwordx4 v[24:27], v[2:3], off offset:2048
	v_add_co_u32_e64 v2, s[0:1], s17, v10
	v_and_b32_e32 v20, 0xffff0000, v20
	s_nop 0
	v_addc_co_u32_e64 v3, s[0:1], 0, v11, s[0:1]
	global_load_dwordx4 v[28:31], v[2:3], off offset:2048
	v_add_co_u32_e64 v2, s[0:1], s18, v10
	v_mul_f32_e32 v20, v20, v20
	s_nop 0
	v_addc_co_u32_e64 v3, s[0:1], 0, v11, s[0:1]
	global_load_dwordx4 v[32:35], v[2:3], off offset:2048
	v_add_co_u32_e64 v2, s[0:1], s19, v10
	v_fmac_f32_e32 v20, v19, v19
	s_nop 0
	v_addc_co_u32_e64 v3, s[0:1], 0, v11, s[0:1]
	v_add_co_u32_e64 v4, s[0:1], s21, v10
	v_lshlrev_b32_e32 v46, 16, v23
	s_nop 0
	v_addc_co_u32_e64 v5, s[0:1], 0, v11, s[0:1]
	v_add_co_u32_e64 v44, s[0:1], s22, v10
	v_and_b32_e32 v23, 0xffff0000, v23
	s_nop 0
	v_addc_co_u32_e64 v45, s[0:1], 0, v11, s[0:1]
	global_load_dwordx4 v[36:39], v[2:3], off offset:2048
	global_load_dwordx4 v[40:43], v[4:5], off offset:2048
	s_nop 0
	global_load_dwordx4 v[2:5], v[44:45], off offset:2048
	v_lshlrev_b32_e32 v44, 16, v21
	v_and_b32_e32 v21, 0xffff0000, v21
	v_fmac_f32_e32 v20, v44, v44
	v_lshlrev_b32_e32 v45, 16, v22
	v_fmac_f32_e32 v20, v21, v21
	v_and_b32_e32 v22, 0xffff0000, v22
	v_fmac_f32_e32 v20, v45, v45
	v_fmac_f32_e32 v20, v22, v22
	v_fmac_f32_e32 v20, v46, v46
	v_fmac_f32_e32 v20, v23, v23
	s_nop 1
	v_mov_b32_dpp v19, v20 row_ror:8 row_mask:0xf bank_mask:0xf
	s_waitcnt lgkmcnt(0)
	v_add_f32_e32 v19, v20, v19
	s_nop 1
	v_mov_b32_dpp v20, v19 row_ror:4 row_mask:0xf bank_mask:0xf
	s_waitcnt lgkmcnt(0)
	v_add_f32_e32 v19, v19, v20
	s_nop 1
	v_mov_b32_dpp v20, v19 quad_perm:[2,3,0,1] row_mask:0xf bank_mask:0xf
	s_waitcnt lgkmcnt(0)
	v_add_f32_e32 v19, v19, v20
	s_nop 1
	v_mov_b32_dpp v20, v19 quad_perm:[1,0,3,2] row_mask:0xf bank_mask:0xf
	s_waitcnt lgkmcnt(0)
	v_add_f32_e32 v19, v19, v20
	s_waitcnt vmcnt(5)
	v_lshlrev_b32_e32 v47, 16, v24
	v_and_b32_e32 v24, 0xffff0000, v24
	v_mul_f32_e32 v24, v24, v24
	v_lshlrev_b32_e32 v48, 16, v25
	v_fmac_f32_e32 v24, v47, v47
	v_and_b32_e32 v25, 0xffff0000, v25
	s_waitcnt vmcnt(4)
	v_lshlrev_b32_e32 v51, 16, v28
	v_and_b32_e32 v28, 0xffff0000, v28
	v_mul_f32_e32 v28, v28, v28
	v_lshlrev_b32_e32 v52, 16, v29
	v_fmac_f32_e32 v28, v51, v51
	v_fmac_f32_e32 v24, v48, v48
	s_waitcnt vmcnt(3)
	v_lshlrev_b32_e32 v55, 16, v32
	v_and_b32_e32 v32, 0xffff0000, v32
	v_mul_f32_e32 v32, v32, v32
	v_lshlrev_b32_e32 v56, 16, v33
	v_fmac_f32_e32 v32, v55, v55
	v_lshlrev_b32_e32 v49, 16, v26
	v_and_b32_e32 v29, 0xffff0000, v29
	v_and_b32_e32 v33, 0xffff0000, v33
	v_fmac_f32_e32 v28, v52, v52
	v_fmac_f32_e32 v32, v56, v56
	v_fmac_f32_e32 v24, v25, v25
	v_and_b32_e32 v26, 0xffff0000, v26
	v_lshlrev_b32_e32 v53, 16, v30
	v_lshlrev_b32_e32 v57, 16, v34
	v_fmac_f32_e32 v28, v29, v29
	v_fmac_f32_e32 v32, v33, v33
	v_fmac_f32_e32 v24, v49, v49
	v_lshlrev_b32_e32 v50, 16, v27
	v_and_b32_e32 v30, 0xffff0000, v30
	v_and_b32_e32 v34, 0xffff0000, v34
	v_fmac_f32_e32 v28, v53, v53
	v_fmac_f32_e32 v32, v57, v57
	v_fmac_f32_e32 v24, v26, v26
	v_and_b32_e32 v27, 0xffff0000, v27
	v_lshlrev_b32_e32 v54, 16, v31
	v_fmac_f32_e32 v28, v30, v30
	v_fmac_f32_e32 v32, v34, v34
	v_fmac_f32_e32 v24, v50, v50
	v_lshlrev_b32_e32 v23, 16, v35
	v_and_b32_e32 v31, 0xffff0000, v31
	v_fmac_f32_e32 v28, v54, v54
	v_fmac_f32_e32 v24, v27, v27
	v_fmac_f32_e32 v32, v23, v23
	v_and_b32_e32 v23, 0xffff0000, v35
	v_fmac_f32_e32 v28, v31, v31
	s_nop 1
	v_mov_b32_dpp v21, v24 row_ror:8 row_mask:0xf bank_mask:0xf
	v_fmac_f32_e32 v32, v23, v23
	s_nop 1
	v_mov_b32_dpp v22, v28 row_ror:8 row_mask:0xf bank_mask:0xf
	s_nop 1
	v_mov_b32_dpp v23, v32 row_ror:8 row_mask:0xf bank_mask:0xf
	s_waitcnt lgkmcnt(2)
	v_add_f32_e32 v21, v24, v21
	s_nop 1
	v_mov_b32_dpp v24, v21 row_ror:4 row_mask:0xf bank_mask:0xf
	s_waitcnt lgkmcnt(2)
	v_add_f32_e32 v22, v28, v22
	s_waitcnt lgkmcnt(1)
	v_add_f32_e32 v23, v32, v23
	s_nop 1
	v_mov_b32_dpp v25, v22 row_ror:4 row_mask:0xf bank_mask:0xf
	s_nop 1
	v_mov_b32_dpp v26, v23 row_ror:4 row_mask:0xf bank_mask:0xf
	s_waitcnt lgkmcnt(2)
	v_add_f32_e32 v21, v21, v24
	s_nop 1
	v_mov_b32_dpp v24, v21 quad_perm:[2,3,0,1] row_mask:0xf bank_mask:0xf
	s_waitcnt vmcnt(1)
	v_and_b32_e32 v28, 0xffff0000, v42
	s_waitcnt lgkmcnt(2)
	v_add_f32_e32 v22, v22, v25
	s_waitcnt lgkmcnt(1)
	v_add_f32_e32 v23, v23, v26
	s_nop 1
	v_mov_b32_dpp v25, v22 quad_perm:[2,3,0,1] row_mask:0xf bank_mask:0xf
	s_nop 1
	v_mov_b32_dpp v26, v23 quad_perm:[2,3,0,1] row_mask:0xf bank_mask:0xf
	s_waitcnt lgkmcnt(2)
	v_add_f32_e32 v21, v21, v24
	s_nop 1
	v_mov_b32_dpp v24, v21 quad_perm:[1,0,3,2] row_mask:0xf bank_mask:0xf
	s_waitcnt lgkmcnt(2)
	v_add_f32_e32 v22, v22, v25
	s_waitcnt lgkmcnt(1)
	v_add_f32_e32 v23, v23, v26
	s_nop 1
	v_mov_b32_dpp v25, v22 quad_perm:[1,0,3,2] row_mask:0xf bank_mask:0xf
	s_nop 1
	v_mov_b32_dpp v26, v23 quad_perm:[1,0,3,2] row_mask:0xf bank_mask:0xf
	s_waitcnt lgkmcnt(2)
	v_add_f32_e32 v20, v21, v24
	v_max3_f32 v19, v19, 0, v20
	v_lshlrev_b32_e32 v24, 16, v36
	s_waitcnt lgkmcnt(1)
	v_add_f32_e32 v20, v22, v25
	s_waitcnt lgkmcnt(0)
	v_add_f32_e32 v21, v23, v26
	v_max3_f32 v19, v19, v20, v21
	v_add_co_u32_e64 v20, s[0:1], s23, v10
	v_and_b32_e32 v25, 0xffff0000, v36
	s_nop 0
	v_addc_co_u32_e64 v21, s[0:1], 0, v11, s[0:1]
	global_load_dwordx4 v[20:23], v[20:21], off offset:2048
	v_mul_f32_e32 v32, v25, v25
	v_fmac_f32_e32 v32, v24, v24
	v_lshlrev_b32_e32 v24, 16, v37
	v_fmac_f32_e32 v32, v24, v24
	v_and_b32_e32 v24, 0xffff0000, v37
	v_fmac_f32_e32 v32, v24, v24
	v_lshlrev_b32_e32 v24, 16, v38
	v_fmac_f32_e32 v32, v24, v24
	v_and_b32_e32 v24, 0xffff0000, v38
	v_fmac_f32_e32 v32, v24, v24
	v_lshlrev_b32_e32 v24, 16, v39
	v_fmac_f32_e32 v32, v24, v24
	v_and_b32_e32 v24, 0xffff0000, v39
	v_and_b32_e32 v25, 0xffff0000, v40
	v_fmac_f32_e32 v32, v24, v24
	v_lshlrev_b32_e32 v24, 16, v40
	v_mul_f32_e32 v34, v25, v25
	v_fmac_f32_e32 v34, v24, v24
	v_lshlrev_b32_e32 v24, 16, v41
	v_fmac_f32_e32 v34, v24, v24
	v_and_b32_e32 v24, 0xffff0000, v41
	v_fmac_f32_e32 v34, v24, v24
	v_lshlrev_b32_e32 v24, 16, v42
	v_fmac_f32_e32 v34, v24, v24
	v_add_co_u32_e64 v24, s[0:1], s25, v10
	v_fmac_f32_e32 v34, v28, v28
	s_nop 0
	v_addc_co_u32_e64 v25, s[0:1], 0, v11, s[0:1]
	global_load_dwordx4 v[24:27], v[24:25], off offset:2048
	v_lshlrev_b32_e32 v28, 16, v43
	v_fmac_f32_e32 v34, v28, v28
	v_and_b32_e32 v28, 0xffff0000, v43
	v_fmac_f32_e32 v34, v28, v28
	s_waitcnt vmcnt(2)
	v_lshlrev_b32_e32 v28, 16, v2
	v_and_b32_e32 v2, 0xffff0000, v2
	v_mul_f32_e32 v2, v2, v2
	v_fmac_f32_e32 v2, v28, v28
	v_lshlrev_b32_e32 v28, 16, v3
	v_fmac_f32_e32 v2, v28, v28
	v_add_co_u32_e64 v28, s[0:1], s30, v10
	v_and_b32_e32 v3, 0xffff0000, v3
	s_nop 0
	v_addc_co_u32_e64 v29, s[0:1], 0, v11, s[0:1]
	v_fmac_f32_e32 v2, v3, v3
	v_lshlrev_b32_e32 v3, 16, v4
	global_load_dwordx4 v[28:31], v[28:29], off offset:2048
	v_fmac_f32_e32 v2, v3, v3
	v_and_b32_e32 v3, 0xffff0000, v4
	v_fmac_f32_e32 v2, v3, v3
	v_lshlrev_b32_e32 v3, 16, v5
	v_fmac_f32_e32 v2, v3, v3
	v_and_b32_e32 v3, 0xffff0000, v5
	v_fmac_f32_e32 v2, v3, v3
	s_nop 1
	v_mov_b32_dpp v3, v2 row_ror:8 row_mask:0xf bank_mask:0xf
	s_nop 1
	v_mov_b32_dpp v33, v32 row_ror:8 row_mask:0xf bank_mask:0xf
	s_nop 1
	v_mov_b32_dpp v35, v34 row_ror:8 row_mask:0xf bank_mask:0xf
	s_waitcnt lgkmcnt(2)
	v_add_f32_e32 v2, v2, v3
	s_nop 1
	v_mov_b32_dpp v3, v2 row_ror:4 row_mask:0xf bank_mask:0xf
	s_waitcnt lgkmcnt(2)
	v_add_f32_e32 v4, v32, v33
	s_nop 1
	v_mov_b32_dpp v5, v4 row_ror:4 row_mask:0xf bank_mask:0xf
	s_waitcnt lgkmcnt(2)
	v_add_f32_e32 v32, v34, v35
	s_nop 1
	v_mov_b32_dpp v33, v32 row_ror:4 row_mask:0xf bank_mask:0xf
	s_waitcnt lgkmcnt(2)
	v_add_f32_e32 v2, v2, v3
	s_nop 1
	v_mov_b32_dpp v3, v2 quad_perm:[2,3,0,1] row_mask:0xf bank_mask:0xf
	s_waitcnt lgkmcnt(2)
	v_add_f32_e32 v4, v4, v5
	s_nop 1
	v_mov_b32_dpp v5, v4 quad_perm:[2,3,0,1] row_mask:0xf bank_mask:0xf
	s_waitcnt lgkmcnt(2)
	v_add_f32_e32 v32, v32, v33
	s_nop 1
	v_mov_b32_dpp v33, v32 quad_perm:[2,3,0,1] row_mask:0xf bank_mask:0xf
	s_waitcnt lgkmcnt(2)
	v_add_f32_e32 v36, v2, v3
	s_nop 1
	v_mov_b32_dpp v37, v36 quad_perm:[1,0,3,2] row_mask:0xf bank_mask:0xf
	s_waitcnt lgkmcnt(2)
	v_add_f32_e32 v34, v4, v5
	s_nop 1
	v_mov_b32_dpp v35, v34 quad_perm:[1,0,3,2] row_mask:0xf bank_mask:0xf
	s_waitcnt lgkmcnt(2)
	v_add_f32_e32 v32, v32, v33
	s_nop 1
	v_mov_b32_dpp v33, v32 quad_perm:[1,0,3,2] row_mask:0xf bank_mask:0xf
	s_waitcnt vmcnt(2)
	v_and_b32_e32 v3, 0xffff0000, v20
	v_lshlrev_b32_e32 v2, 16, v20
	v_mul_f32_e32 v20, v3, v3
	v_fmac_f32_e32 v20, v2, v2
	v_lshlrev_b32_e32 v2, 16, v21
	v_fmac_f32_e32 v20, v2, v2
	v_add_co_u32_e64 v2, s[0:1], s31, v10
	v_and_b32_e32 v21, 0xffff0000, v21
	s_nop 0
	v_addc_co_u32_e64 v3, s[0:1], 0, v11, s[0:1]
	global_load_dwordx4 v[2:5], v[2:3], off offset:2048
	v_fmac_f32_e32 v20, v21, v21
	v_lshlrev_b32_e32 v21, 16, v22
	v_fmac_f32_e32 v20, v21, v21
	v_and_b32_e32 v21, 0xffff0000, v22
	v_fmac_f32_e32 v20, v21, v21
	v_lshlrev_b32_e32 v21, 16, v23
	v_fmac_f32_e32 v20, v21, v21
	v_and_b32_e32 v21, 0xffff0000, v23
	v_fmac_f32_e32 v20, v21, v21
	s_nop 1
	v_mov_b32_dpp v21, v20 row_ror:8 row_mask:0xf bank_mask:0xf
	s_waitcnt lgkmcnt(1)
	v_add_f32_e32 v23, v32, v33
	v_add_f32_e32 v22, v34, v35
	v_max3_f32 v19, v19, v22, v23
	v_add_f32_e32 v32, v36, v37
	s_waitcnt lgkmcnt(0)
	v_add_f32_e32 v33, v20, v21
	v_add_co_u32_e64 v20, s[0:1], s34, v10
	s_nop 1
	v_mov_b32_dpp v34, v33 row_ror:4 row_mask:0xf bank_mask:0xf
	s_nop 0
	v_addc_co_u32_e64 v21, s[0:1], 0, v11, s[0:1]
	global_load_dwordx4 v[20:23], v[20:21], off offset:2048
	s_waitcnt vmcnt(3)
	v_lshlrev_b32_e32 v35, 16, v24
	v_and_b32_e32 v24, 0xffff0000, v24
	v_mul_f32_e32 v36, v24, v24
	v_fmac_f32_e32 v36, v35, v35
	v_lshlrev_b32_e32 v24, 16, v25
	v_fmac_f32_e32 v36, v24, v24
	v_and_b32_e32 v24, 0xffff0000, v25
	v_fmac_f32_e32 v36, v24, v24
	v_lshlrev_b32_e32 v24, 16, v26
	v_fmac_f32_e32 v36, v24, v24
	v_and_b32_e32 v24, 0xffff0000, v26
	v_fmac_f32_e32 v36, v24, v24
	v_lshlrev_b32_e32 v24, 16, v27
	v_fmac_f32_e32 v36, v24, v24
	v_and_b32_e32 v24, 0xffff0000, v27
	s_waitcnt vmcnt(2)
	v_and_b32_e32 v25, 0xffff0000, v28
	v_fmac_f32_e32 v36, v24, v24
	v_lshlrev_b32_e32 v24, 16, v28
	v_mul_f32_e32 v28, v25, v25
	v_fmac_f32_e32 v28, v24, v24
	v_lshlrev_b32_e32 v24, 16, v29
	v_fmac_f32_e32 v28, v24, v24
	v_and_b32_e32 v24, 0xffff0000, v29
	v_fmac_f32_e32 v28, v24, v24
	v_lshlrev_b32_e32 v24, 16, v30
	v_fmac_f32_e32 v28, v24, v24
	v_and_b32_e32 v29, 0xffff0000, v30
	v_fmac_f32_e32 v28, v29, v29
	v_lshlrev_b32_e32 v29, 16, v31
	v_fmac_f32_e32 v28, v29, v29
	v_and_b32_e32 v29, 0xffff0000, v31
	v_fmac_f32_e32 v28, v29, v29
	s_nop 1
	v_mov_b32_dpp v29, v28 row_ror:8 row_mask:0xf bank_mask:0xf
	s_nop 1
	v_mov_b32_dpp v35, v36 row_ror:8 row_mask:0xf bank_mask:0xf
	s_waitcnt lgkmcnt(2)
	v_add_f32_e32 v30, v33, v34
	s_nop 1
	v_mov_b32_dpp v31, v30 quad_perm:[2,3,0,1] row_mask:0xf bank_mask:0xf
	v_add_co_u32_e64 v24, s[0:1], s35, v10
	s_waitcnt lgkmcnt(2)
	v_add_f32_e32 v28, v28, v29
	s_nop 1
	v_mov_b32_dpp v29, v28 row_ror:4 row_mask:0xf bank_mask:0xf
	v_addc_co_u32_e64 v25, s[0:1], 0, v11, s[0:1]
	s_waitcnt lgkmcnt(2)
	v_add_f32_e32 v33, v36, v35
	s_nop 1
	v_mov_b32_dpp v34, v33 row_ror:4 row_mask:0xf bank_mask:0xf
	s_waitcnt lgkmcnt(1)
	v_add_f32_e32 v28, v28, v29
	s_nop 1
	v_mov_b32_dpp v29, v28 quad_perm:[2,3,0,1] row_mask:0xf bank_mask:0xf
	v_add_f32_e32 v30, v30, v31
	s_nop 1
	v_mov_b32_dpp v31, v30 quad_perm:[1,0,3,2] row_mask:0xf bank_mask:0xf
	s_waitcnt lgkmcnt(2)
	v_add_f32_e32 v33, v33, v34
	s_nop 1
	v_mov_b32_dpp v34, v33 quad_perm:[2,3,0,1] row_mask:0xf bank_mask:0xf
	s_waitcnt lgkmcnt(2)
	v_add_f32_e32 v38, v28, v29
	global_load_dwordx4 v[24:27], v[24:25], off offset:2048
	s_waitcnt lgkmcnt(1)
	v_add_f32_e32 v30, v30, v31
	v_max3_f32 v19, v19, v32, v30
	s_waitcnt lgkmcnt(0)
	v_add_f32_e32 v36, v33, v34
	s_nop 1
	v_mov_b32_dpp v37, v36 quad_perm:[1,0,3,2] row_mask:0xf bank_mask:0xf
	s_nop 1
	v_mov_b32_dpp v39, v38 quad_perm:[1,0,3,2] row_mask:0xf bank_mask:0xf
	s_waitcnt vmcnt(2)
	v_lshlrev_b32_e32 v28, 16, v2
	v_and_b32_e32 v2, 0xffff0000, v2
	v_mul_f32_e32 v40, v2, v2
	v_fmac_f32_e32 v40, v28, v28
	v_lshlrev_b32_e32 v2, 16, v3
	v_fmac_f32_e32 v40, v2, v2
	v_and_b32_e32 v2, 0xffff0000, v3
	v_fmac_f32_e32 v40, v2, v2
	v_lshlrev_b32_e32 v2, 16, v4
	v_fmac_f32_e32 v40, v2, v2
	v_and_b32_e32 v2, 0xffff0000, v4
	v_add_co_u32_e64 v28, s[0:1], s42, v10
	v_fmac_f32_e32 v40, v2, v2
	v_lshlrev_b32_e32 v2, 16, v5
	v_addc_co_u32_e64 v29, s[0:1], 0, v11, s[0:1]
	v_fmac_f32_e32 v40, v2, v2
	v_and_b32_e32 v2, 0xffff0000, v5
	v_fmac_f32_e32 v40, v2, v2
	v_add_co_u32_e64 v2, s[0:1], s43, v10
	s_waitcnt vmcnt(1)
	v_lshlrev_b32_e32 v32, 16, v20
	v_addc_co_u32_e64 v3, s[0:1], 0, v11, s[0:1]
	global_load_dwordx4 v[2:5], v[2:3], off offset:2048
	v_and_b32_e32 v20, 0xffff0000, v20
	v_mul_f32_e32 v20, v20, v20
	v_add_co_u32_e64 v10, s[0:1], s48, v10
	global_load_dwordx4 v[28:31], v[28:29], off offset:2048
	v_fmac_f32_e32 v20, v32, v32
	v_lshlrev_b32_e32 v32, 16, v21
	v_addc_co_u32_e64 v11, s[0:1], 0, v11, s[0:1]
	v_fmac_f32_e32 v20, v32, v32
	global_load_dwordx4 v[32:35], v[10:11], off offset:2048
	s_nop 1
	v_mov_b32_dpp v41, v40 row_ror:8 row_mask:0xf bank_mask:0xf
	v_and_b32_e32 v21, 0xffff0000, v21
	v_fmac_f32_e32 v20, v21, v21
	v_lshlrev_b32_e32 v21, 16, v22
	v_fmac_f32_e32 v20, v21, v21
	v_and_b32_e32 v21, 0xffff0000, v22
	v_fmac_f32_e32 v20, v21, v21
	v_lshlrev_b32_e32 v21, 16, v23
	v_fmac_f32_e32 v20, v21, v21
	v_and_b32_e32 v10, 0xffff0000, v23
	s_waitcnt lgkmcnt(0)
	v_add_f32_e32 v22, v40, v41
	v_fmac_f32_e32 v20, v10, v10
	s_nop 1
	v_mov_b32_dpp v23, v22 row_ror:4 row_mask:0xf bank_mask:0xf
	s_nop 1
	v_mov_b32_dpp v10, v20 row_ror:8 row_mask:0xf bank_mask:0xf
	v_add_f32_e32 v11, v36, v37
	v_add_f32_e32 v21, v38, v39
	v_max3_f32 v11, v19, v11, v21
	s_waitcnt lgkmcnt(1)
	v_add_f32_e32 v22, v22, v23
	s_waitcnt lgkmcnt(0)
	v_add_f32_e32 v10, v20, v10
	s_nop 1
	v_mov_b32_dpp v23, v22 quad_perm:[2,3,0,1] row_mask:0xf bank_mask:0xf
	s_nop 1
	v_mov_b32_dpp v20, v10 row_ror:4 row_mask:0xf bank_mask:0xf
	s_waitcnt lgkmcnt(1)
	v_add_f32_e32 v22, v22, v23
	s_waitcnt lgkmcnt(0)
	v_add_f32_e32 v10, v10, v20
	s_nop 1
	v_mov_b32_dpp v23, v22 quad_perm:[1,0,3,2] row_mask:0xf bank_mask:0xf
	s_nop 1
	v_mov_b32_dpp v20, v10 quad_perm:[2,3,0,1] row_mask:0xf bank_mask:0xf
	s_waitcnt lgkmcnt(1)
	v_add_f32_e32 v19, v22, v23
	s_waitcnt lgkmcnt(0)
	v_add_f32_e32 v10, v10, v20
	s_nop 1
	v_mov_b32_dpp v20, v10 quad_perm:[1,0,3,2] row_mask:0xf bank_mask:0xf
	s_waitcnt vmcnt(3)
	v_lshlrev_b32_e32 v36, 16, v24
	v_and_b32_e32 v24, 0xffff0000, v24
	v_mul_f32_e32 v24, v24, v24
	s_waitcnt lgkmcnt(0)
	v_add_f32_e32 v10, v10, v20
	v_fmac_f32_e32 v24, v36, v36
	v_lshlrev_b32_e32 v36, 16, v25
	v_fmac_f32_e32 v24, v36, v36
	v_and_b32_e32 v25, 0xffff0000, v25
	v_fmac_f32_e32 v24, v25, v25
	v_lshlrev_b32_e32 v25, 16, v26
	v_fmac_f32_e32 v24, v25, v25
	v_and_b32_e32 v25, 0xffff0000, v26
	v_fmac_f32_e32 v24, v25, v25
	v_lshlrev_b32_e32 v25, 16, v27
	v_fmac_f32_e32 v24, v25, v25
	v_and_b32_e32 v25, 0xffff0000, v27
	v_fmac_f32_e32 v24, v25, v25
	s_nop 1
	v_mov_b32_dpp v25, v24 row_ror:8 row_mask:0xf bank_mask:0xf
	v_max3_f32 v10, v11, v19, v10
	s_waitcnt lgkmcnt(0)
	v_add_f32_e32 v24, v24, v25
	s_nop 1
	v_mov_b32_dpp v25, v24 row_ror:4 row_mask:0xf bank_mask:0xf
	s_waitcnt lgkmcnt(0)
	v_add_f32_e32 v24, v24, v25
	s_nop 1
	v_mov_b32_dpp v25, v24 quad_perm:[2,3,0,1] row_mask:0xf bank_mask:0xf
	s_waitcnt vmcnt(2)
	v_lshlrev_b32_e32 v22, 16, v2
	v_and_b32_e32 v2, 0xffff0000, v2
	v_mul_f32_e32 v2, v2, v2
	v_fmac_f32_e32 v2, v22, v22
	v_lshlrev_b32_e32 v22, 16, v3
	v_fmac_f32_e32 v2, v22, v22
	v_and_b32_e32 v3, 0xffff0000, v3
	v_fmac_f32_e32 v2, v3, v3
	v_lshlrev_b32_e32 v3, 16, v4
	v_fmac_f32_e32 v2, v3, v3
	v_and_b32_e32 v3, 0xffff0000, v4
	s_waitcnt vmcnt(1)
	v_and_b32_e32 v21, 0xffff0000, v28
	v_fmac_f32_e32 v2, v3, v3
	v_lshlrev_b32_e32 v3, 16, v5
	v_lshlrev_b32_e32 v20, 16, v28
	v_mul_f32_e32 v21, v21, v21
	v_fmac_f32_e32 v2, v3, v3
	v_and_b32_e32 v3, 0xffff0000, v5
	s_waitcnt vmcnt(0)
	v_and_b32_e32 v5, 0xffff0000, v32
	v_fmac_f32_e32 v21, v20, v20
	v_lshlrev_b32_e32 v20, 16, v29
	v_lshlrev_b32_e32 v4, 16, v32
	v_mul_f32_e32 v5, v5, v5
	v_fmac_f32_e32 v21, v20, v20
	v_and_b32_e32 v20, 0xffff0000, v29
	v_fmac_f32_e32 v5, v4, v4
	v_lshlrev_b32_e32 v4, 16, v33
	v_fmac_f32_e32 v21, v20, v20
	v_lshlrev_b32_e32 v20, 16, v30
	v_fmac_f32_e32 v5, v4, v4
	v_and_b32_e32 v4, 0xffff0000, v33
	v_fmac_f32_e32 v21, v20, v20
	v_and_b32_e32 v20, 0xffff0000, v30
	v_fmac_f32_e32 v5, v4, v4
	v_lshlrev_b32_e32 v4, 16, v34
	v_fmac_f32_e32 v21, v20, v20
	v_lshlrev_b32_e32 v20, 16, v31
	v_fmac_f32_e32 v5, v4, v4
	v_and_b32_e32 v4, 0xffff0000, v34
	v_fmac_f32_e32 v21, v20, v20
	v_and_b32_e32 v20, 0xffff0000, v31
	v_fmac_f32_e32 v5, v4, v4
	v_lshlrev_b32_e32 v4, 16, v35
	v_fmac_f32_e32 v21, v20, v20
	v_fmac_f32_e32 v5, v4, v4
	v_and_b32_e32 v4, 0xffff0000, v35
	s_nop 1
	v_mov_b32_dpp v20, v21 row_ror:8 row_mask:0xf bank_mask:0xf
	v_fmac_f32_e32 v2, v3, v3
	v_fmac_f32_e32 v5, v4, v4
	s_nop 1
	v_mov_b32_dpp v3, v2 row_ror:8 row_mask:0xf bank_mask:0xf
	s_nop 1
	v_mov_b32_dpp v4, v5 row_ror:8 row_mask:0xf bank_mask:0xf
	s_waitcnt lgkmcnt(2)
	v_add_f32_e32 v20, v21, v20
	s_nop 1
	v_mov_b32_dpp v21, v20 row_ror:4 row_mask:0xf bank_mask:0xf
	v_add_f32_e32 v11, v24, v25
	s_waitcnt lgkmcnt(2)
	v_add_f32_e32 v2, v2, v3
	s_waitcnt lgkmcnt(1)
	v_add_f32_e32 v4, v5, v4
	s_nop 1
	v_mov_b32_dpp v3, v2 row_ror:4 row_mask:0xf bank_mask:0xf
	s_nop 1
	v_mov_b32_dpp v5, v4 row_ror:4 row_mask:0xf bank_mask:0xf
	s_waitcnt lgkmcnt(2)
	v_add_f32_e32 v20, v20, v21
	s_nop 1
	v_mov_b32_dpp v21, v20 quad_perm:[2,3,0,1] row_mask:0xf bank_mask:0xf
	s_nop 1
	v_mov_b32_dpp v19, v11 quad_perm:[1,0,3,2] row_mask:0xf bank_mask:0xf
	s_waitcnt lgkmcnt(3)
	v_add_f32_e32 v2, v2, v3
	s_waitcnt lgkmcnt(2)
	v_add_f32_e32 v4, v4, v5
	s_nop 1
	v_mov_b32_dpp v3, v2 quad_perm:[2,3,0,1] row_mask:0xf bank_mask:0xf
	s_nop 1
	v_mov_b32_dpp v5, v4 quad_perm:[2,3,0,1] row_mask:0xf bank_mask:0xf
	s_waitcnt lgkmcnt(3)
	v_add_f32_e32 v20, v20, v21
	s_nop 1
	v_mov_b32_dpp v21, v20 quad_perm:[1,0,3,2] row_mask:0xf bank_mask:0xf
	s_waitcnt lgkmcnt(3)
	v_add_f32_e32 v11, v11, v19
	s_waitcnt lgkmcnt(2)
	v_add_f32_e32 v2, v2, v3
	s_waitcnt lgkmcnt(1)
	v_add_f32_e32 v4, v4, v5
	s_nop 1
	v_mov_b32_dpp v3, v2 quad_perm:[1,0,3,2] row_mask:0xf bank_mask:0xf
	s_nop 1
	v_mov_b32_dpp v5, v4 quad_perm:[1,0,3,2] row_mask:0xf bank_mask:0xf
	s_waitcnt lgkmcnt(2)
	v_add_f32_e32 v19, v20, v21
	v_max3_f32 v10, v10, v11, v19
	s_waitcnt lgkmcnt(1)
	v_add_f32_e32 v2, v2, v3
	s_waitcnt lgkmcnt(0)
	v_add_f32_e32 v3, v4, v5
	v_max3_f32 v2, v10, v2, v3
	ds_bpermute_b32 v3, v12, v2
	s_waitcnt lgkmcnt(0)
	v_max_f32_e32 v3, v3, v3
	v_max_f32_e32 v2, v2, v3
	ds_bpermute_b32 v3, v13, v2
	s_and_saveexec_b64 s[0:1], vcc
	s_cbranch_execz .LBB0_346
	s_waitcnt lgkmcnt(0)
	v_max_f32_e32 v3, v3, v3
	v_max_f32_e32 v2, v2, v2
	v_max_f32_e32 v2, v2, v3
	global_store_dword v7, v2, s[10:11]
	s_branch .LBB0_346
